# MoE weight conversion split re-balanced: 40960 items beside the selected attention (was 49000), the rest with the router phase
# speedup vs baseline: 1.0168x; 1.0050x over previous
.LBB0_995:
	s_cmp_lg_u32 s89, 0
	s_cbranch_scc1 .LBB0_1002
	s_andn2_b64 vcc, exec, s[10:11]
	s_cbranch_vccnz .LBB0_1002
	s_sub_i32 s0, s82, s15
	s_lshl_b32 s25, s0, 3
	s_add_i32 s25, s25, s92
	s_cmpk_gt_u32 s25, 0x9fff
	s_cbranch_scc1 .LBB0_1002
	s_sub_i32 s0, s88, s15
	s_lshl_b32 s8, s0, 3
	s_add_u32 s9, s86, 0x50000000
	s_mul_i32 s0, s92, 0x4100
	s_addc_u32 s10, s87, 0
	s_load_dwordx2 s[4:5], s[90:91], 0xa0
	s_load_dwordx2 s[6:7], s[90:91], 0xb0
	s_add_i32 s2, s0, 0
	s_lshl_b32 s0, s25, 6
	s_lshl_b32 s1, s25, 5
	s_and_b32 s1, s1, 0x780
	s_and_b32 s0, s0, 64
	v_lshlrev_b32_e32 v0, 2, v1
	s_or_b32 s0, s1, s0
	s_waitcnt vmcnt(3)
	v_and_b32_e32 v142, 60, v0
	v_or_b32_e32 v0, s0, v142
	v_readlane_b32 s0, v255, 4
	s_bitcmp0_b32 s0, 7
	s_waitcnt lgkmcnt(0)
	s_cselect_b32 s1, s5, s7
	s_cselect_b32 s0, s4, s6
	s_lshl_b32 s3, s25, 13
	s_and_b32 s3, s3, 0x1f000000
	s_add_u32 s0, s0, s3
	s_addc_u32 s1, s1, 0
	s_and_b32 s3, s25, 0x7c0
	v_lshrrev_b32_e32 v143, 4, v1
	s_waitcnt vmcnt(0)
	v_or_b32_e32 v4, s3, v143
	v_lshlrev_b32_e32 v130, 2, v0
	v_mov_b32_e32 v131, 0
	v_lshl_add_u64 v[2:3], s[0:1], 0, v[130:131]
	v_lshlrev_b32_e32 v130, 13, v4
	v_lshl_add_u64 v[2:3], v[2:3], 0, v[130:131]
	s_mov_b32 s11, 0x8000
	v_add_co_u32_e32 v4, vcc, s11, v2
	s_mov_b32 s12, 0x10000
	s_nop 0
	v_addc_co_u32_e32 v5, vcc, 0, v3, vcc
	global_load_dwordx4 v[66:69], v[2:3], off nt
	global_load_dwordx4 v[70:73], v[4:5], off nt
	v_add_co_u32_e32 v4, vcc, s12, v2
	s_mov_b32 s13, 0x18000
	s_nop 0
	v_addc_co_u32_e32 v5, vcc, 0, v3, vcc
	v_add_co_u32_e32 v6, vcc, s13, v2
	s_mov_b32 s14, 0x20000
	s_nop 0
	v_addc_co_u32_e32 v7, vcc, 0, v3, vcc
	global_load_dwordx4 v[74:77], v[4:5], off nt
	global_load_dwordx4 v[78:81], v[6:7], off nt
	v_add_co_u32_e32 v4, vcc, s14, v2
	s_mov_b32 s16, 0x28000
	s_nop 0
	v_addc_co_u32_e32 v5, vcc, 0, v3, vcc
	v_add_co_u32_e32 v6, vcc, s16, v2
	s_mov_b32 s17, 0x30000
	s_nop 0
	v_addc_co_u32_e32 v7, vcc, 0, v3, vcc
	global_load_dwordx4 v[82:85], v[4:5], off nt
	global_load_dwordx4 v[86:89], v[6:7], off nt
	v_add_co_u32_e32 v4, vcc, s17, v2
	s_mov_b32 s18, 0x38000
	s_nop 0
	v_addc_co_u32_e32 v5, vcc, 0, v3, vcc
	v_add_co_u32_e32 v6, vcc, s18, v2
	s_mov_b32 s19, 0x40000
	s_nop 0
	v_addc_co_u32_e32 v7, vcc, 0, v3, vcc
	global_load_dwordx4 v[90:93], v[4:5], off nt
	global_load_dwordx4 v[94:97], v[6:7], off nt
	v_add_co_u32_e32 v4, vcc, s19, v2
	s_mov_b32 s20, 0x48000
	s_nop 0
	v_addc_co_u32_e32 v5, vcc, 0, v3, vcc
	v_add_co_u32_e32 v6, vcc, s20, v2
	s_mov_b32 s21, 0x50000
	s_nop 0
	v_addc_co_u32_e32 v7, vcc, 0, v3, vcc
	global_load_dwordx4 v[98:101], v[4:5], off nt
	global_load_dwordx4 v[102:105], v[6:7], off nt
	v_add_co_u32_e32 v4, vcc, s21, v2
	s_mov_b32 s22, 0x58000
	s_nop 0
	v_addc_co_u32_e32 v5, vcc, 0, v3, vcc
	v_add_co_u32_e32 v6, vcc, s22, v2
	s_mov_b32 s0, 0x60000
	s_nop 0
	v_addc_co_u32_e32 v7, vcc, 0, v3, vcc
	global_load_dwordx4 v[106:109], v[4:5], off nt
	global_load_dwordx4 v[110:113], v[6:7], off nt
	v_add_co_u32_e32 v4, vcc, s0, v2
	s_mov_b32 s0, 0x68000
	s_nop 0
	v_addc_co_u32_e32 v5, vcc, 0, v3, vcc
	v_add_co_u32_e32 v6, vcc, s0, v2
	s_mov_b32 s0, 0x70000
	s_nop 0
	v_addc_co_u32_e32 v7, vcc, 0, v3, vcc
	global_load_dwordx4 v[114:117], v[4:5], off nt
	global_load_dwordx4 v[118:121], v[6:7], off nt
	v_add_co_u32_e32 v4, vcc, s0, v2
	s_mov_b32 s0, 0x78000
	s_nop 0
	v_addc_co_u32_e32 v5, vcc, 0, v3, vcc
	v_add_co_u32_e32 v2, vcc, s0, v2
	s_lshl_b32 s0, s15, 3
	s_nop 0
	v_addc_co_u32_e32 v3, vcc, 0, v3, vcc
	global_load_dwordx4 v[122:125], v[4:5], off nt
	global_load_dwordx4 v[126:129], v[2:3], off nt
	s_sub_i32 s23, 0, s0
	s_lshl_b32 s0, s82, 3
	v_lshlrev_b32_e32 v3, 4, v1
	s_add_i32 s24, s92, s0
	s_lshl_b32 s0, s88, 7
	s_lshl_b32 s1, s15, 7
	v_and_b32_e32 v132, 48, v3
	s_sub_i32 s26, s0, s1
	s_lshl_b32 s0, s88, 3
	s_lshl_b32 s1, s15, 4
	v_mul_u32_u24_e32 v3, 0x104, v132
	v_and_b32_e32 v4, 60, v1
	s_sub_i32 s27, s0, s1
	s_add_i32 s0, s24, s0
	v_add3_u32 v144, s2, v3, v4
	v_lshlrev_b32_e32 v3, 5, v1
	s_sub_i32 s0, s0, s1
	v_lshl_add_u32 v0, v142, 2, s2
	v_mul_u32_u24_e32 v2, 0x104, v143
	v_and_b32_e32 v134, 0x780, v3
	s_lshl_b32 s28, s0, 6
	s_lshl_b32 s0, s88, 9
	s_lshl_b32 s1, s15, 9
	v_mov_b32_e32 v133, v131
	v_mov_b32_e32 v135, v131
	v_or_b32_e32 v136, 0x800, v134
	v_mov_b32_e32 v137, v131
	v_or_b32_e32 v138, 0x1000, v134
	v_mov_b32_e32 v139, v131
	v_or_b32_e32 v140, 0x1800, v134
	v_mov_b32_e32 v141, v131
	s_lshl_b32 s25, s25, 4
	s_sub_i32 s15, s0, s1
	v_add_u32_e32 v145, v0, v2
	s_branch .LBB0_1000
.LBB0_999:
	v_add_u32_e32 v0, 0x410, v145
	s_waitcnt vmcnt(31)
	ds_write2_b32 v145, v66, v67 offset1:1
	ds_write2_b32 v145, v68, v69 offset0:2 offset1:3
	s_waitcnt vmcnt(30)
	ds_write2_b32 v0, v70, v71 offset1:1
	v_add_u32_e32 v0, 0x418, v145
	ds_write2_b32 v0, v72, v73 offset1:1
	v_add_u32_e32 v0, 0x820, v145
	s_waitcnt vmcnt(29)
	ds_write2_b32 v0, v74, v75 offset1:1
	v_add_u32_e32 v0, 0x828, v145
	ds_write2_b32 v0, v76, v77 offset1:1
	v_add_u32_e32 v0, 0xc30, v145
	s_waitcnt vmcnt(28)
	ds_write2_b32 v0, v78, v79 offset1:1
	v_add_u32_e32 v0, 0xc38, v145
	ds_write2_b32 v0, v80, v81 offset1:1
	v_add_u32_e32 v0, 0x1040, v145
	s_waitcnt vmcnt(27)
	ds_write2_b32 v0, v82, v83 offset1:1
	v_add_u32_e32 v0, 0x1048, v145
	ds_write2_b32 v0, v84, v85 offset1:1
	v_add_u32_e32 v0, 0x1450, v145
	s_waitcnt vmcnt(26)
	ds_write2_b32 v0, v86, v87 offset1:1
	v_add_u32_e32 v0, 0x1458, v145
	ds_write2_b32 v0, v88, v89 offset1:1
	v_add_u32_e32 v0, 0x1860, v145
	s_waitcnt vmcnt(25)
	ds_write2_b32 v0, v90, v91 offset1:1
	v_add_u32_e32 v0, 0x1868, v145
	ds_write2_b32 v0, v92, v93 offset1:1
	v_add_u32_e32 v0, 0x1c70, v145
	s_waitcnt vmcnt(24)
	ds_write2_b32 v0, v94, v95 offset1:1
	v_add_u32_e32 v0, 0x1c78, v145
	ds_write2_b32 v0, v96, v97 offset1:1
	v_add_u32_e32 v0, 0x2080, v145
	s_waitcnt vmcnt(23)
	ds_write2_b32 v0, v98, v99 offset1:1
	v_add_u32_e32 v0, 0x2088, v145
	ds_write2_b32 v0, v100, v101 offset1:1
	v_add_u32_e32 v0, 0x2490, v145
	s_waitcnt vmcnt(22)
	ds_write2_b32 v0, v102, v103 offset1:1
	v_add_u32_e32 v0, 0x2498, v145
	ds_write2_b32 v0, v104, v105 offset1:1
	v_add_u32_e32 v0, 0x28a0, v145
	s_waitcnt vmcnt(21)
	ds_write2_b32 v0, v106, v107 offset1:1
	v_add_u32_e32 v0, 0x28a8, v145
	ds_write2_b32 v0, v108, v109 offset1:1
	v_add_u32_e32 v0, 0x2cb0, v145
	s_waitcnt vmcnt(20)
	ds_write2_b32 v0, v110, v111 offset1:1
	v_add_u32_e32 v0, 0x2cb8, v145
	ds_write2_b32 v0, v112, v113 offset1:1
	v_add_u32_e32 v0, 0x30c0, v145
	s_waitcnt vmcnt(19)
	ds_write2_b32 v0, v114, v115 offset1:1
	v_add_u32_e32 v0, 0x30c8, v145
	ds_write2_b32 v0, v116, v117 offset1:1
	v_add_u32_e32 v0, 0x34d0, v145
	s_waitcnt vmcnt(18)
	ds_write2_b32 v0, v118, v119 offset1:1
	v_add_u32_e32 v0, 0x34d8, v145
	ds_write2_b32 v0, v120, v121 offset1:1
	v_add_u32_e32 v0, 0x38e0, v145
	s_waitcnt vmcnt(17)
	ds_write2_b32 v0, v122, v123 offset1:1
	v_add_u32_e32 v0, 0x38e8, v145
	ds_write2_b32 v0, v124, v125 offset1:1
	v_add_u32_e32 v0, 0x3cf0, v145
	s_waitcnt vmcnt(16)
	ds_write2_b32 v0, v126, v127 offset1:1
	v_add_u32_e32 v0, 0x3cf8, v145
	ds_write2_b32 v0, v128, v129 offset1:1
	s_waitcnt lgkmcnt(0)
	ds_read2_b32 v[70:71], v144 offset1:16
	ds_read2_b32 v[72:73], v144 offset0:65 offset1:81
	ds_read2_b32 v[74:75], v144 offset0:130 offset1:146
	ds_read2_b32 v[76:77], v144 offset0:195 offset1:211
	v_mov_b32_e32 v66, 0
	s_waitcnt lgkmcnt(3)
	v_mul_f32_e32 v0, 0x43800000, v70
	s_waitcnt lgkmcnt(2)
	v_mul_f32_e32 v67, 0x43800000, v72
	v_cvt_pk_fp8_f32 v66, v0, v67
	v_add_u32_e32 v0, 0x400, v144
	ds_read2_b32 v[78:79], v0 offset0:4 offset1:20
	ds_read2_b32 v[80:81], v0 offset0:69 offset1:85
	ds_read2_b32 v[82:83], v0 offset0:134 offset1:150
	s_waitcnt lgkmcnt(4)
	v_mul_f32_e32 v68, 0x43800000, v74
	s_waitcnt lgkmcnt(3)
	v_mul_f32_e32 v67, 0x43800000, v76
	ds_read2_b32 v[84:85], v0 offset0:199 offset1:215
	v_add_u32_e32 v106, 0x800, v144
	v_cvt_pk_fp8_f32 v66, v68, v67 op_sel:[0,0,1]
	s_waitcnt lgkmcnt(3)
	v_mul_f32_e32 v68, 0x43800000, v78
	s_waitcnt lgkmcnt(2)
	v_mul_f32_e32 v69, 0x43800000, v80
	v_mov_b32_e32 v67, 0
	ds_read2_b32 v[86:87], v106 offset0:8 offset1:24
	ds_read2_b32 v[88:89], v106 offset0:73 offset1:89
	v_add_u32_e32 v107, 0xc00, v144
	v_cvt_pk_fp8_f32 v67, v68, v69
	ds_read2_b32 v[90:91], v106 offset0:138 offset1:154
	ds_read2_b32 v[92:93], v106 offset0:203 offset1:219
	ds_read2_b32 v[94:95], v107 offset0:12 offset1:28
	ds_read2_b32 v[96:97], v107 offset0:77 offset1:93
	s_ashr_i32 s0, s29, 11
	s_ashr_i32 s1, s0, 31
	s_lshl_b64 s[0:1], s[0:1], 23
	s_waitcnt lgkmcnt(7)
	v_mul_f32_e32 v70, 0x43800000, v82
	s_waitcnt lgkmcnt(6)
	v_mul_f32_e32 v68, 0x43800000, v84
	s_add_u32 s0, s9, s0
	v_cvt_pk_fp8_f32 v67, v70, v68 op_sel:[0,0,1]
	s_waitcnt lgkmcnt(5)
	v_mul_f32_e32 v69, 0x43800000, v86
	s_waitcnt lgkmcnt(4)
	v_mul_f32_e32 v70, 0x43800000, v88
	v_mov_b32_e32 v68, 0
	ds_read2_b32 v[98:99], v107 offset0:142 offset1:158
	ds_read2_b32 v[100:101], v107 offset0:207 offset1:223
	s_addc_u32 s1, s10, s1
	s_and_b32 s2, s25, 0x3f0
	s_bfe_u32 s3, s29, 0x40007
	v_cvt_pk_fp8_f32 v68, v69, v70
	s_waitcnt lgkmcnt(3)
	v_mul_f32_e32 v70, 0x43800000, v94
	s_waitcnt lgkmcnt(2)
	v_mul_f32_e32 v76, 0x43800000, v96
	v_mov_b32_e32 v69, 0
	s_or_b32 s2, s2, s3
	v_cvt_pk_fp8_f32 v69, v70, v76
	s_lshl_b32 s2, s2, 13
	s_add_u32 s0, s0, s2
	v_mul_f32_e32 v72, 0x43800000, v90
	v_mul_f32_e32 v74, 0x43800000, v92
	s_addc_u32 s1, s1, 0
	s_and_b32 s2, s29, 64
	v_cvt_pk_fp8_f32 v68, v72, v74 op_sel:[0,0,1]
	s_waitcnt lgkmcnt(1)
	v_mul_f32_e32 v70, 0x43800000, v98
	s_waitcnt lgkmcnt(0)
	v_mul_f32_e32 v72, 0x43800000, v100
	s_add_u32 s0, s0, s2
	v_cvt_pk_fp8_f32 v69, v70, v72 op_sel:[0,0,1]
	s_addc_u32 s1, s1, 0
	v_lshl_add_u64 v[102:103], s[0:1], 0, v[132:133]
	v_lshl_add_u64 v[104:105], v[102:103], 0, v[134:135]
	global_store_dwordx4 v[104:105], v[66:69], off nt
	v_mul_f32_e32 v70, 0x43800000, v77
	v_mul_f32_e32 v72, 0x43800000, v93
	v_mul_f32_e32 v67, 0x43800000, v71
	v_mul_f32_e32 v68, 0x43800000, v73
	v_mov_b32_e32 v66, 0
	v_cvt_pk_fp8_f32 v66, v67, v68
	v_mul_f32_e32 v68, 0x43800000, v79
	v_mul_f32_e32 v71, 0x43800000, v81
	v_mov_b32_e32 v67, 0
	v_cvt_pk_fp8_f32 v67, v68, v71
	v_mul_f32_e32 v69, 0x43800000, v75
	v_cvt_pk_fp8_f32 v66, v69, v70 op_sel:[0,0,1]
	v_mul_f32_e32 v68, 0x43800000, v83
	v_mul_f32_e32 v69, 0x43800000, v85
	v_cvt_pk_fp8_f32 v67, v68, v69 op_sel:[0,0,1]
	v_mul_f32_e32 v69, 0x43800000, v87
	v_mul_f32_e32 v70, 0x43800000, v89
	v_mov_b32_e32 v68, 0
	v_cvt_pk_fp8_f32 v68, v69, v70
	v_mul_f32_e32 v70, 0x43800000, v95
	v_mul_f32_e32 v73, 0x43800000, v97
	v_mov_b32_e32 v69, 0
	v_cvt_pk_fp8_f32 v69, v70, v73
	v_mul_f32_e32 v71, 0x43800000, v91
	v_cvt_pk_fp8_f32 v68, v71, v72 op_sel:[0,0,1]
	v_mul_f32_e32 v70, 0x43800000, v99
	v_mul_f32_e32 v71, 0x43800000, v101
	v_cvt_pk_fp8_f32 v69, v70, v71 op_sel:[0,0,1]
	ds_read2_b32 v[70:71], v144 offset0:32 offset1:48
	ds_read2_b32 v[72:73], v144 offset0:97 offset1:113
	ds_read2_b32 v[74:75], v144 offset0:162 offset1:178
	v_lshl_add_u64 v[76:77], v[102:103], 0, v[136:137]
	s_add_i32 s24, s24, s8
	global_store_dwordx4 v[76:77], v[66:69], off nt
	ds_read2_b32 v[76:77], v144 offset0:227 offset1:243
	ds_read2_b32 v[78:79], v0 offset0:36 offset1:52
	ds_read2_b32 v[80:81], v0 offset0:101 offset1:117
	s_waitcnt lgkmcnt(5)
	v_mul_f32_e32 v67, 0x43800000, v70
	s_waitcnt lgkmcnt(4)
	v_mul_f32_e32 v68, 0x43800000, v72
	v_mov_b32_e32 v66, 0
	v_cvt_pk_fp8_f32 v66, v67, v68
	s_waitcnt lgkmcnt(3)
	v_mul_f32_e32 v69, 0x43800000, v74
	s_waitcnt lgkmcnt(2)
	v_mul_f32_e32 v67, 0x43800000, v76
	ds_read2_b32 v[82:83], v0 offset0:166 offset1:182
	ds_read2_b32 v[84:85], v0 offset0:231 offset1:247
	v_cvt_pk_fp8_f32 v66, v69, v67 op_sel:[0,0,1]
	s_waitcnt lgkmcnt(3)
	v_mul_f32_e32 v68, 0x43800000, v78
	s_waitcnt lgkmcnt(2)
	v_mul_f32_e32 v69, 0x43800000, v80
	v_mov_b32_e32 v67, 0
	ds_read2_b32 v[86:87], v106 offset0:40 offset1:56
	v_cvt_pk_fp8_f32 v67, v68, v69
	ds_read2_b32 v[88:89], v106 offset0:105 offset1:121
	ds_read2_b32 v[90:91], v106 offset0:170 offset1:186
	ds_read2_b32 v[92:93], v106 offset0:235 offset1:251
	ds_read2_b32 v[94:95], v107 offset0:44 offset1:60
	ds_read2_b32 v[96:97], v107 offset0:109 offset1:125
	s_waitcnt lgkmcnt(7)
	v_mul_f32_e32 v0, 0x43800000, v82
	s_waitcnt lgkmcnt(6)
	v_mul_f32_e32 v68, 0x43800000, v84
	v_cvt_pk_fp8_f32 v67, v0, v68 op_sel:[0,0,1]
	s_waitcnt lgkmcnt(5)
	v_mul_f32_e32 v0, 0x43800000, v86
	s_waitcnt lgkmcnt(4)
	v_mul_f32_e32 v69, 0x43800000, v88
	v_mov_b32_e32 v68, 0
	ds_read2_b32 v[98:99], v107 offset0:174 offset1:190
	ds_read2_b32 v[100:101], v107 offset0:239 offset1:255
	v_cvt_pk_fp8_f32 v68, v0, v69
	s_waitcnt lgkmcnt(3)
	v_mul_f32_e32 v0, 0x43800000, v94
	s_waitcnt lgkmcnt(2)
	v_mul_f32_e32 v74, 0x43800000, v96
	v_mov_b32_e32 v69, 0
	v_cvt_pk_fp8_f32 v69, v0, v74
	v_mul_f32_e32 v70, 0x43800000, v90
	v_mul_f32_e32 v72, 0x43800000, v92
	v_cvt_pk_fp8_f32 v68, v70, v72 op_sel:[0,0,1]
	s_waitcnt lgkmcnt(1)
	v_mul_f32_e32 v0, 0x43800000, v98
	s_waitcnt lgkmcnt(0)
	v_mul_f32_e32 v70, 0x43800000, v100
	v_cvt_pk_fp8_f32 v69, v0, v70 op_sel:[0,0,1]
	v_mul_f32_e32 v0, 0x43800000, v71
	v_mul_f32_e32 v71, 0x43800000, v73
	v_mov_b32_e32 v70, 0
	v_cvt_pk_fp8_f32 v70, v0, v71
	v_mul_f32_e32 v0, 0x43800000, v79
	v_mul_f32_e32 v74, 0x43800000, v81
	v_mov_b32_e32 v71, 0
	v_cvt_pk_fp8_f32 v71, v0, v74
	v_mul_f32_e32 v72, 0x43800000, v75
	v_mul_f32_e32 v73, 0x43800000, v77
	v_cvt_pk_fp8_f32 v70, v72, v73 op_sel:[0,0,1]
	v_mul_f32_e32 v0, 0x43800000, v83
	v_mul_f32_e32 v72, 0x43800000, v85
	v_cvt_pk_fp8_f32 v71, v0, v72 op_sel:[0,0,1]
	v_mul_f32_e32 v0, 0x43800000, v87
	v_mul_f32_e32 v73, 0x43800000, v89
	v_mov_b32_e32 v72, 0
	v_cvt_pk_fp8_f32 v72, v0, v73
	v_mul_f32_e32 v0, 0x43800000, v95
	v_mul_f32_e32 v76, 0x43800000, v97
	v_mov_b32_e32 v73, 0
	v_cvt_pk_fp8_f32 v73, v0, v76
	v_mul_f32_e32 v74, 0x43800000, v91
	v_mul_f32_e32 v75, 0x43800000, v93
	v_cvt_pk_fp8_f32 v72, v74, v75 op_sel:[0,0,1]
	v_mul_f32_e32 v0, 0x43800000, v99
	v_mul_f32_e32 v74, 0x43800000, v101
	v_cvt_pk_fp8_f32 v73, v0, v74 op_sel:[0,0,1]
	v_lshl_add_u64 v[74:75], v[102:103], 0, v[138:139]
	global_store_dwordx4 v[74:75], v[66:69], off nt
	s_add_i32 s0, s23, s24
	s_add_i32 s25, s25, s26
	v_lshl_add_u64 v[66:67], v[102:103], 0, v[140:141]
	global_store_dwordx4 v[66:67], v[70:73], off nt
	s_waitcnt lgkmcnt(0)
	s_add_i32 s28, s28, s15
	s_waitcnt vmcnt(4)
	v_mov_b64_e32 v[68:69], v[4:5]
	v_mov_b64_e32 v[72:73], v[8:9]
	v_mov_b64_e32 v[76:77], v[12:13]
	v_mov_b64_e32 v[80:81], v[16:17]
	v_mov_b64_e32 v[84:85], v[20:21]
	v_mov_b64_e32 v[88:89], v[24:25]
	v_mov_b64_e32 v[92:93], v[28:29]
	v_mov_b64_e32 v[96:97], v[32:33]
	v_mov_b64_e32 v[100:101], v[36:37]
	v_mov_b64_e32 v[104:105], v[40:41]
	v_mov_b64_e32 v[108:109], v[44:45]
	v_mov_b64_e32 v[112:113], v[48:49]
	v_mov_b64_e32 v[116:117], v[52:53]
	v_mov_b64_e32 v[120:121], v[56:57]
	v_mov_b64_e32 v[124:125], v[60:61]
	v_mov_b64_e32 v[128:129], v[64:65]
	s_cmp_lt_i32 s0, 0xa000
	v_mov_b64_e32 v[66:67], v[2:3]
	v_mov_b64_e32 v[70:71], v[6:7]
	v_mov_b64_e32 v[74:75], v[10:11]
	v_mov_b64_e32 v[78:79], v[14:15]
	v_mov_b64_e32 v[82:83], v[18:19]
	v_mov_b64_e32 v[86:87], v[22:23]
	v_mov_b64_e32 v[90:91], v[26:27]
	v_mov_b64_e32 v[94:95], v[30:31]
	v_mov_b64_e32 v[98:99], v[34:35]
	v_mov_b64_e32 v[102:103], v[38:39]
	v_mov_b64_e32 v[106:107], v[42:43]
	v_mov_b64_e32 v[110:111], v[46:47]
	v_mov_b64_e32 v[114:115], v[50:51]
	v_mov_b64_e32 v[118:119], v[54:55]
	v_mov_b64_e32 v[122:123], v[58:59]
	v_mov_b64_e32 v[126:127], v[62:63]
	s_cbranch_scc0 .LBB0_1002
.LBB0_1000:
	s_add_i32 s29, s23, s24
	s_add_i32 s30, s27, s24
	s_cmp_gt_i32 s30, 0x9fff
	s_cbranch_scc1 .Lcv4_last
	s_lshr_b32 s1, s28, 1
	s_ashr_i32 s0, s30, 11
	s_and_b32 s2, s1, 0x780
	s_and_b32 s3, s28, 64
	s_bitcmp0_b32 s29, 1
	s_cselect_b32 s31, s5, s7
	s_cselect_b32 s33, s4, s6
	s_ashr_i32 s1, s0, 31
	s_lshl_b64 s[0:1], s[0:1], 24
	s_add_u32 s0, s33, s0
	s_addc_u32 s1, s31, s1
	s_or_b32 s2, s3, s2
	v_or_b32_e32 v0, s2, v142
	s_and_b32 s2, s30, 0x7c0
	v_or_b32_e32 v4, s2, v143
	v_lshlrev_b32_e32 v130, 2, v0
	v_lshl_add_u64 v[2:3], s[0:1], 0, v[130:131]
	v_lshlrev_b32_e32 v130, 13, v4
	v_lshl_add_u64 v[58:59], v[2:3], 0, v[130:131]
	v_add_co_u32_e32 v10, vcc, s11, v58
	s_nop 1
	v_addc_co_u32_e32 v11, vcc, 0, v59, vcc
	global_load_dwordx4 v[2:5], v[58:59], off nt
	global_load_dwordx4 v[6:9], v[10:11], off nt
	v_add_co_u32_e32 v10, vcc, s12, v58
	s_nop 1
	v_addc_co_u32_e32 v11, vcc, 0, v59, vcc
	v_add_co_u32_e32 v14, vcc, s13, v58
	s_nop 1
	v_addc_co_u32_e32 v15, vcc, 0, v59, vcc
	v_add_co_u32_e32 v18, vcc, s14, v58
	global_load_dwordx4 v[10:13], v[10:11], off nt
	s_nop 0
	global_load_dwordx4 v[14:17], v[14:15], off nt
	v_addc_co_u32_e32 v19, vcc, 0, v59, vcc
	v_add_co_u32_e32 v22, vcc, s16, v58
	s_nop 1
	v_addc_co_u32_e32 v23, vcc, 0, v59, vcc
	v_add_co_u32_e32 v26, vcc, s17, v58
	global_load_dwordx4 v[18:21], v[18:19], off nt
	s_nop 0
	global_load_dwordx4 v[22:25], v[22:23], off nt
	v_addc_co_u32_e32 v27, vcc, 0, v59, vcc
	v_add_co_u32_e32 v30, vcc, s18, v58
	s_nop 1
	v_addc_co_u32_e32 v31, vcc, 0, v59, vcc
	v_add_co_u32_e32 v34, vcc, s19, v58
	global_load_dwordx4 v[26:29], v[26:27], off nt
	s_nop 0
	global_load_dwordx4 v[30:33], v[30:31], off nt
	v_addc_co_u32_e32 v35, vcc, 0, v59, vcc
	v_add_co_u32_e32 v38, vcc, s20, v58
	s_nop 1
	v_addc_co_u32_e32 v39, vcc, 0, v59, vcc
	v_add_co_u32_e32 v42, vcc, s21, v58
	global_load_dwordx4 v[34:37], v[34:35], off nt
	s_nop 0
	global_load_dwordx4 v[38:41], v[38:39], off nt
	v_addc_co_u32_e32 v43, vcc, 0, v59, vcc
	v_add_co_u32_e32 v46, vcc, s22, v58
	s_nop 1
	v_addc_co_u32_e32 v47, vcc, 0, v59, vcc
	v_add_co_u32_e32 v50, vcc, 0x60000, v58
	global_load_dwordx4 v[42:45], v[42:43], off nt
	s_nop 0
	global_load_dwordx4 v[46:49], v[46:47], off nt
	v_addc_co_u32_e32 v51, vcc, 0, v59, vcc
	v_add_co_u32_e32 v54, vcc, 0x68000, v58
	s_nop 1
	v_addc_co_u32_e32 v55, vcc, 0, v59, vcc
	v_add_co_u32_e32 v60, vcc, 0x70000, v58
	global_load_dwordx4 v[50:53], v[50:51], off nt
	s_nop 0
	global_load_dwordx4 v[54:57], v[54:55], off nt
	v_addc_co_u32_e32 v61, vcc, 0, v59, vcc
	v_add_co_u32_e32 v62, vcc, 0x78000, v58
	s_nop 1
	v_addc_co_u32_e32 v63, vcc, 0, v59, vcc
	global_load_dwordx4 v[58:61], v[60:61], off nt
	s_nop 0
	global_load_dwordx4 v[62:65], v[62:63], off nt
	s_branch .LBB0_999

.LBB0_1311:
	s_lshl_b32 s0, s82, 2
	s_add_i32 s0, s0, s92
	s_add_i32 s0, s0, -4
	s_cmpk_gt_u32 s1, 0xff
	s_cselect_b32 s14, s0, -1
	s_cmp_lt_i32 s14, 0
	s_cbranch_scc1 .LBB0_1329
	s_cmpk_gt_u32 s88, 0xe0
	s_mov_b32 s0, 0x10000
	s_cselect_b32 s0, s0, 0x16000
	s_cmpk_gt_i32 s88, 0xab
	s_cselect_b32 s1, 0xa000, 0
	s_cselect_b32 s18, s0, 0x18000
	s_add_i32 s19, s14, s1
	s_cmp_ge_u32 s19, s18
	s_cbranch_scc1 .LBB0_1329
	s_load_dwordx2 s[4:5], s[90:91], 0xa0
	s_load_dwordx2 s[6:7], s[90:91], 0xb0
	s_load_dwordx2 s[8:9], s[90:91], 0xc0
	s_cmpk_gt_u32 s19, 0xffff
	v_readfirstlane_b32 s34, v0
	s_waitcnt vmcnt(0)
	v_lshlrev_b32_e32 v2, 2, v1
	s_cbranch_scc0 .LBB0_1315
	s_add_i32 s34, s19, 0xffff0000
	s_lshr_b32 s0, s34, 10
	s_mov_b32 s1, 0
	s_lshl_b64 s[0:1], s[0:1], 24
	s_waitcnt lgkmcnt(0)
	s_add_u32 s10, s8, s0
	s_addc_u32 s11, s9, s1
	s_lshl_b32 s1, s19, 6
	s_lshl_b32 s0, s19, 1
	s_and_b32 s1, s1, 0x7c0
	v_and_b32_e32 v142, 60, v2
	v_or_b32_e32 v130, s1, v142
	v_mov_b32_e32 v143, s0
	v_mov_b32_e32 v3, v143
	s_cbranch_execz .LBB0_1316
	s_branch .LBB0_1317
